# combo + P0 silu staging loads batched (16 loads in flight instead of load-wait x16)
# speedup vs baseline: 1.0127x; 1.0069x over previous
.LBB0_10:
	global_load_dword v112, v[2:3], off
	v_lshl_add_u64 v[2:3], v[2:3], 0, s[6:7]
	global_load_dword v113, v[2:3], off
	v_lshl_add_u64 v[2:3], v[2:3], 0, s[6:7]
	global_load_dword v114, v[2:3], off
	v_lshl_add_u64 v[2:3], v[2:3], 0, s[6:7]
	global_load_dword v115, v[2:3], off
	v_lshl_add_u64 v[2:3], v[2:3], 0, s[6:7]
	global_load_dword v116, v[2:3], off
	v_lshl_add_u64 v[2:3], v[2:3], 0, s[6:7]
	global_load_dword v117, v[2:3], off
	v_lshl_add_u64 v[2:3], v[2:3], 0, s[6:7]
	global_load_dword v118, v[2:3], off
	v_lshl_add_u64 v[2:3], v[2:3], 0, s[6:7]
	global_load_dword v119, v[2:3], off
	v_lshl_add_u64 v[2:3], v[2:3], 0, s[6:7]
	global_load_dword v120, v[2:3], off
	v_lshl_add_u64 v[2:3], v[2:3], 0, s[6:7]
	global_load_dword v121, v[2:3], off
	v_lshl_add_u64 v[2:3], v[2:3], 0, s[6:7]
	global_load_dword v122, v[2:3], off
	v_lshl_add_u64 v[2:3], v[2:3], 0, s[6:7]
	global_load_dword v123, v[2:3], off
	v_lshl_add_u64 v[2:3], v[2:3], 0, s[6:7]
	global_load_dword v124, v[2:3], off
	v_lshl_add_u64 v[2:3], v[2:3], 0, s[6:7]
	global_load_dword v125, v[2:3], off
	v_lshl_add_u64 v[2:3], v[2:3], 0, s[6:7]
	global_load_dword v126, v[2:3], off
	v_lshl_add_u64 v[2:3], v[2:3], 0, s[6:7]
	global_load_dword v127, v[2:3], off
	s_waitcnt vmcnt(15)
	v_mov_b32_e32 v6, v112
	v_mul_f32_e32 v7, 0xbfb8aa3b, v6
	v_exp_f32_e32 v7, v7
	s_nop 0
	v_add_f32_e32 v7, 1.0, v7
	v_div_scale_f32 v8, s[16:17], v7, v7, v6
	v_rcp_f32_e32 v9, v8
	v_div_scale_f32 v10, vcc, v6, v7, v6
	v_fma_f32 v11, -v8, v9, 1.0
	v_fmac_f32_e32 v9, v11, v9
	v_mul_f32_e32 v11, v10, v9
	v_fma_f32 v12, -v8, v11, v10
	v_fmac_f32_e32 v11, v12, v9
	v_fma_f32 v8, -v8, v11, v10
	v_div_fmas_f32 v8, v8, v9, v11
	v_div_fixup_f32 v6, v8, v7, v6
	ds_write_b32 v5, v6
	v_add_u32_e32 v5, 0x800, v5
	s_waitcnt vmcnt(14)
	v_mov_b32_e32 v6, v113
	v_mul_f32_e32 v7, 0xbfb8aa3b, v6
	v_exp_f32_e32 v7, v7
	s_nop 0
	v_add_f32_e32 v7, 1.0, v7
	v_div_scale_f32 v8, s[16:17], v7, v7, v6
	v_rcp_f32_e32 v9, v8
	v_div_scale_f32 v10, vcc, v6, v7, v6
	v_fma_f32 v11, -v8, v9, 1.0
	v_fmac_f32_e32 v9, v11, v9
	v_mul_f32_e32 v11, v10, v9
	v_fma_f32 v12, -v8, v11, v10
	v_fmac_f32_e32 v11, v12, v9
	v_fma_f32 v8, -v8, v11, v10
	v_div_fmas_f32 v8, v8, v9, v11
	v_div_fixup_f32 v6, v8, v7, v6
	ds_write_b32 v5, v6
	v_add_u32_e32 v5, 0x800, v5
	s_waitcnt vmcnt(13)
	v_mov_b32_e32 v6, v114
	v_mul_f32_e32 v7, 0xbfb8aa3b, v6
	v_exp_f32_e32 v7, v7
	s_nop 0
	v_add_f32_e32 v7, 1.0, v7
	v_div_scale_f32 v8, s[16:17], v7, v7, v6
	v_rcp_f32_e32 v9, v8
	v_div_scale_f32 v10, vcc, v6, v7, v6
	v_fma_f32 v11, -v8, v9, 1.0
	v_fmac_f32_e32 v9, v11, v9
	v_mul_f32_e32 v11, v10, v9
	v_fma_f32 v12, -v8, v11, v10
	v_fmac_f32_e32 v11, v12, v9
	v_fma_f32 v8, -v8, v11, v10
	v_div_fmas_f32 v8, v8, v9, v11
	v_div_fixup_f32 v6, v8, v7, v6
	ds_write_b32 v5, v6
	v_add_u32_e32 v5, 0x800, v5
	s_waitcnt vmcnt(12)
	v_mov_b32_e32 v6, v115
	v_mul_f32_e32 v7, 0xbfb8aa3b, v6
	v_exp_f32_e32 v7, v7
	s_nop 0
	v_add_f32_e32 v7, 1.0, v7
	v_div_scale_f32 v8, s[16:17], v7, v7, v6
	v_rcp_f32_e32 v9, v8
	v_div_scale_f32 v10, vcc, v6, v7, v6
	v_fma_f32 v11, -v8, v9, 1.0
	v_fmac_f32_e32 v9, v11, v9
	v_mul_f32_e32 v11, v10, v9
	v_fma_f32 v12, -v8, v11, v10
	v_fmac_f32_e32 v11, v12, v9
	v_fma_f32 v8, -v8, v11, v10
	v_div_fmas_f32 v8, v8, v9, v11
	v_div_fixup_f32 v6, v8, v7, v6
	ds_write_b32 v5, v6
	v_add_u32_e32 v5, 0x800, v5
	s_waitcnt vmcnt(11)
	v_mov_b32_e32 v6, v116
	v_mul_f32_e32 v7, 0xbfb8aa3b, v6
	v_exp_f32_e32 v7, v7
	s_nop 0
	v_add_f32_e32 v7, 1.0, v7
	v_div_scale_f32 v8, s[16:17], v7, v7, v6
	v_rcp_f32_e32 v9, v8
	v_div_scale_f32 v10, vcc, v6, v7, v6
	v_fma_f32 v11, -v8, v9, 1.0
	v_fmac_f32_e32 v9, v11, v9
	v_mul_f32_e32 v11, v10, v9
	v_fma_f32 v12, -v8, v11, v10
	v_fmac_f32_e32 v11, v12, v9
	v_fma_f32 v8, -v8, v11, v10
	v_div_fmas_f32 v8, v8, v9, v11
	v_div_fixup_f32 v6, v8, v7, v6
	ds_write_b32 v5, v6
	v_add_u32_e32 v5, 0x800, v5
	s_waitcnt vmcnt(10)
	v_mov_b32_e32 v6, v117
	v_mul_f32_e32 v7, 0xbfb8aa3b, v6
	v_exp_f32_e32 v7, v7
	s_nop 0
	v_add_f32_e32 v7, 1.0, v7
	v_div_scale_f32 v8, s[16:17], v7, v7, v6
	v_rcp_f32_e32 v9, v8
	v_div_scale_f32 v10, vcc, v6, v7, v6
	v_fma_f32 v11, -v8, v9, 1.0
	v_fmac_f32_e32 v9, v11, v9
	v_mul_f32_e32 v11, v10, v9
	v_fma_f32 v12, -v8, v11, v10
	v_fmac_f32_e32 v11, v12, v9
	v_fma_f32 v8, -v8, v11, v10
	v_div_fmas_f32 v8, v8, v9, v11
	v_div_fixup_f32 v6, v8, v7, v6
	ds_write_b32 v5, v6
	v_add_u32_e32 v5, 0x800, v5
	s_waitcnt vmcnt(9)
	v_mov_b32_e32 v6, v118
	v_mul_f32_e32 v7, 0xbfb8aa3b, v6
	v_exp_f32_e32 v7, v7
	s_nop 0
	v_add_f32_e32 v7, 1.0, v7
	v_div_scale_f32 v8, s[16:17], v7, v7, v6
	v_rcp_f32_e32 v9, v8
	v_div_scale_f32 v10, vcc, v6, v7, v6
	v_fma_f32 v11, -v8, v9, 1.0
	v_fmac_f32_e32 v9, v11, v9
	v_mul_f32_e32 v11, v10, v9
	v_fma_f32 v12, -v8, v11, v10
	v_fmac_f32_e32 v11, v12, v9
	v_fma_f32 v8, -v8, v11, v10
	v_div_fmas_f32 v8, v8, v9, v11
	v_div_fixup_f32 v6, v8, v7, v6
	ds_write_b32 v5, v6
	v_add_u32_e32 v5, 0x800, v5
	s_waitcnt vmcnt(8)
	v_mov_b32_e32 v6, v119
	v_mul_f32_e32 v7, 0xbfb8aa3b, v6
	v_exp_f32_e32 v7, v7
	s_nop 0
	v_add_f32_e32 v7, 1.0, v7
	v_div_scale_f32 v8, s[16:17], v7, v7, v6
	v_rcp_f32_e32 v9, v8
	v_div_scale_f32 v10, vcc, v6, v7, v6
	v_fma_f32 v11, -v8, v9, 1.0
	v_fmac_f32_e32 v9, v11, v9
	v_mul_f32_e32 v11, v10, v9
	v_fma_f32 v12, -v8, v11, v10
	v_fmac_f32_e32 v11, v12, v9
	v_fma_f32 v8, -v8, v11, v10
	v_div_fmas_f32 v8, v8, v9, v11
	v_div_fixup_f32 v6, v8, v7, v6
	ds_write_b32 v5, v6
	v_add_u32_e32 v5, 0x800, v5
	s_waitcnt vmcnt(7)
	v_mov_b32_e32 v6, v120
	v_mul_f32_e32 v7, 0xbfb8aa3b, v6
	v_exp_f32_e32 v7, v7
	s_nop 0
	v_add_f32_e32 v7, 1.0, v7
	v_div_scale_f32 v8, s[16:17], v7, v7, v6
	v_rcp_f32_e32 v9, v8
	v_div_scale_f32 v10, vcc, v6, v7, v6
	v_fma_f32 v11, -v8, v9, 1.0
	v_fmac_f32_e32 v9, v11, v9
	v_mul_f32_e32 v11, v10, v9
	v_fma_f32 v12, -v8, v11, v10
	v_fmac_f32_e32 v11, v12, v9
	v_fma_f32 v8, -v8, v11, v10
	v_div_fmas_f32 v8, v8, v9, v11
	v_div_fixup_f32 v6, v8, v7, v6
	ds_write_b32 v5, v6
	v_add_u32_e32 v5, 0x800, v5
	s_waitcnt vmcnt(6)
	v_mov_b32_e32 v6, v121
	v_mul_f32_e32 v7, 0xbfb8aa3b, v6
	v_exp_f32_e32 v7, v7
	s_nop 0
	v_add_f32_e32 v7, 1.0, v7
	v_div_scale_f32 v8, s[16:17], v7, v7, v6
	v_rcp_f32_e32 v9, v8
	v_div_scale_f32 v10, vcc, v6, v7, v6
	v_fma_f32 v11, -v8, v9, 1.0
	v_fmac_f32_e32 v9, v11, v9
	v_mul_f32_e32 v11, v10, v9
	v_fma_f32 v12, -v8, v11, v10
	v_fmac_f32_e32 v11, v12, v9
	v_fma_f32 v8, -v8, v11, v10
	v_div_fmas_f32 v8, v8, v9, v11
	v_div_fixup_f32 v6, v8, v7, v6
	ds_write_b32 v5, v6
	v_add_u32_e32 v5, 0x800, v5
	s_waitcnt vmcnt(5)
	v_mov_b32_e32 v6, v122
	v_mul_f32_e32 v7, 0xbfb8aa3b, v6
	v_exp_f32_e32 v7, v7
	s_nop 0
	v_add_f32_e32 v7, 1.0, v7
	v_div_scale_f32 v8, s[16:17], v7, v7, v6
	v_rcp_f32_e32 v9, v8
	v_div_scale_f32 v10, vcc, v6, v7, v6
	v_fma_f32 v11, -v8, v9, 1.0
	v_fmac_f32_e32 v9, v11, v9
	v_mul_f32_e32 v11, v10, v9
	v_fma_f32 v12, -v8, v11, v10
	v_fmac_f32_e32 v11, v12, v9
	v_fma_f32 v8, -v8, v11, v10
	v_div_fmas_f32 v8, v8, v9, v11
	v_div_fixup_f32 v6, v8, v7, v6
	ds_write_b32 v5, v6
	v_add_u32_e32 v5, 0x800, v5
	s_waitcnt vmcnt(4)
	v_mov_b32_e32 v6, v123
	v_mul_f32_e32 v7, 0xbfb8aa3b, v6
	v_exp_f32_e32 v7, v7
	s_nop 0
	v_add_f32_e32 v7, 1.0, v7
	v_div_scale_f32 v8, s[16:17], v7, v7, v6
	v_rcp_f32_e32 v9, v8
	v_div_scale_f32 v10, vcc, v6, v7, v6
	v_fma_f32 v11, -v8, v9, 1.0
	v_fmac_f32_e32 v9, v11, v9
	v_mul_f32_e32 v11, v10, v9
	v_fma_f32 v12, -v8, v11, v10
	v_fmac_f32_e32 v11, v12, v9
	v_fma_f32 v8, -v8, v11, v10
	v_div_fmas_f32 v8, v8, v9, v11
	v_div_fixup_f32 v6, v8, v7, v6
	ds_write_b32 v5, v6
	v_add_u32_e32 v5, 0x800, v5
	s_waitcnt vmcnt(3)
	v_mov_b32_e32 v6, v124
	v_mul_f32_e32 v7, 0xbfb8aa3b, v6
	v_exp_f32_e32 v7, v7
	s_nop 0
	v_add_f32_e32 v7, 1.0, v7
	v_div_scale_f32 v8, s[16:17], v7, v7, v6
	v_rcp_f32_e32 v9, v8
	v_div_scale_f32 v10, vcc, v6, v7, v6
	v_fma_f32 v11, -v8, v9, 1.0
	v_fmac_f32_e32 v9, v11, v9
	v_mul_f32_e32 v11, v10, v9
	v_fma_f32 v12, -v8, v11, v10
	v_fmac_f32_e32 v11, v12, v9
	v_fma_f32 v8, -v8, v11, v10
	v_div_fmas_f32 v8, v8, v9, v11
	v_div_fixup_f32 v6, v8, v7, v6
	ds_write_b32 v5, v6
	v_add_u32_e32 v5, 0x800, v5
	s_waitcnt vmcnt(2)
	v_mov_b32_e32 v6, v125
	v_mul_f32_e32 v7, 0xbfb8aa3b, v6
	v_exp_f32_e32 v7, v7
	s_nop 0
	v_add_f32_e32 v7, 1.0, v7
	v_div_scale_f32 v8, s[16:17], v7, v7, v6
	v_rcp_f32_e32 v9, v8
	v_div_scale_f32 v10, vcc, v6, v7, v6
	v_fma_f32 v11, -v8, v9, 1.0
	v_fmac_f32_e32 v9, v11, v9
	v_mul_f32_e32 v11, v10, v9
	v_fma_f32 v12, -v8, v11, v10
	v_fmac_f32_e32 v11, v12, v9
	v_fma_f32 v8, -v8, v11, v10
	v_div_fmas_f32 v8, v8, v9, v11
	v_div_fixup_f32 v6, v8, v7, v6
	ds_write_b32 v5, v6
	v_add_u32_e32 v5, 0x800, v5
	s_waitcnt vmcnt(1)
	v_mov_b32_e32 v6, v126
	v_mul_f32_e32 v7, 0xbfb8aa3b, v6
	v_exp_f32_e32 v7, v7
	s_nop 0
	v_add_f32_e32 v7, 1.0, v7
	v_div_scale_f32 v8, s[16:17], v7, v7, v6
	v_rcp_f32_e32 v9, v8
	v_div_scale_f32 v10, vcc, v6, v7, v6
	v_fma_f32 v11, -v8, v9, 1.0
	v_fmac_f32_e32 v9, v11, v9
	v_mul_f32_e32 v11, v10, v9
	v_fma_f32 v12, -v8, v11, v10
	v_fmac_f32_e32 v11, v12, v9
	v_fma_f32 v8, -v8, v11, v10
	v_div_fmas_f32 v8, v8, v9, v11
	v_div_fixup_f32 v6, v8, v7, v6
	ds_write_b32 v5, v6
	v_add_u32_e32 v5, 0x800, v5
	s_waitcnt vmcnt(0)
	v_mov_b32_e32 v6, v127
	v_mul_f32_e32 v7, 0xbfb8aa3b, v6
	v_exp_f32_e32 v7, v7
	s_nop 0
	v_add_f32_e32 v7, 1.0, v7
	v_div_scale_f32 v8, s[16:17], v7, v7, v6
	v_rcp_f32_e32 v9, v8
	v_div_scale_f32 v10, vcc, v6, v7, v6
	v_fma_f32 v11, -v8, v9, 1.0
	v_fmac_f32_e32 v9, v11, v9
	v_mul_f32_e32 v11, v10, v9
	v_fma_f32 v12, -v8, v11, v10
	v_fmac_f32_e32 v11, v12, v9
	v_fma_f32 v8, -v8, v11, v10
	v_div_fmas_f32 v8, v8, v9, v11
	v_div_fixup_f32 v6, v8, v7, v6
	ds_write_b32 v5, v6
	v_add_u32_e32 v5, 0x800, v5
